# all of the conversion inside the attention loop (one unit every 2nd iteration)
# baseline (speedup 1.0000x reference)
; #define LAS __attribute__((address_space(3)))
; __device__ __forceinline__ void convert_experts(Frame& F, int lo, int hi) {
;     const int gw = F.vcu * 8 + F.wave, NGW = F.G * 8;
;     LAS unsigned char* scr = F.lds + F.wave * 16384;
;     unsigned char* W1t = WSP(F, WS_W1T, unsigned char); unsigned char* W2t = WSP(F, WS_W2T, unsigned char);
;     const float* weg = F.a->in[I_WEG]; const float* weu = F.a->in[I_WEU]; const float* wed = F.a->in[I_WED];
;     const float* wsg = F.a->in[I_WSG]; const float* wsu = F.a->in[I_WSU]; const float* wsd = F.a->in[I_WSD];
;     ...
;     constexpr int NPAIRS = CONV_ITEMS / 2;
;     (void)lo; (void)hi;
;     ...
;     if (gw < NPAIRS) {
;         const int ns = 2 * ((NPAIRS - gw + NGW - 1) / NGW);
;         int sq = 0, r = CONV_RIDX(0);
;         TItem tc, tn; CONV_DESC(r, tc); tn = tc;
;         int p = 0; bool first = true;
;         titem_issue(tc, F.lane, scr);
;         for (;;) {
;             const bool more = sq + 1 < ns; const int rn = more ? CONV_RIDX(sq + 1) : r;
;             if (more) { CONV_DESC(rn, tn); titem_issue(tn, F.lane, scr + (p ^ 1) * 8192); }
;             if (!more) asm volatile("s_waitcnt vmcnt(0)" ::: "memory");
;             else if (first) asm volatile("s_waitcnt vmcnt(8)" ::: "memory");
;             else asm volatile("s_waitcnt vmcnt(12)" ::: "memory");
;             titem_finish(tc, F.lane, scr + p * 8192);
;             asm volatile("s_waitcnt lgkmcnt(0)" ::: "memory");
;             if (!more) break;
;             tc = tn; r = rn; ++sq; p ^= 1; first = false;
;         }
;     }
.Lcv1_vcu:
	s_lshl_b32 s11, s11, 3
	s_add_u32 s89, s11, s9
	s_lshl_b32 s71, s8, 3
	s_mul_i32 s10, s71, 24
	s_add_u32 s89, s89, s10
	s_mov_b32 s69, s89
	s_add_u32 s86, s84, 0x9180000
	s_addc_u32 s87, s85, 0
	s_add_u32 s84, s84, 0x1100000
	s_addc_u32 s85, s85, 0
	s_mov_b32 s90, 0xc2b8aa3b
	s_cmp_ge_u32 s89, 49344
	s_cbranch_scc1 .Lcv1_done
	s_cmp_lt_u32 s69, 49344
	s_cbranch_scc0 .Lcv1_dummyA1
	s_lshr_b32 s10, s69, 6
	s_and_b32 s12, s69, 63
	s_mul_hi_u32 s14, s10, 0xaaaaaaab
	s_lshr_b32 s14, s14, 1
	s_mul_i32 s11, s14, 3
	s_sub_u32 s11, s10, s11
	s_cmp_lt_u32 s14, 256
	s_cselect_b32 s10, s14, 0
	s_cselect_b64 s[44:45], -1, 0
	s_lshl_b32 s10, s10, 20
	s_cmp_eq_u32 s11, 2
	s_cbranch_scc1 .Lcv1_downA1
	s_cmp_eq_u32 s11, 0
	s_cselect_b64 s[4:5], s[72:73], s[74:75]
	s_cselect_b64 s[38:39], s[78:79], s[80:81]
	s_mov_b32 s94, 0xc3317218
	s_cselect_b32 s94, s90, s94
	s_cmp_lg_u64 s[44:45], 0
	s_cselect_b64 s[4:5], s[4:5], s[38:39]
	s_lshr_b32 s38, s12, 3
	s_and_b32 s39, s12, 7
	s_lshl_b32 s8, s38, 17
	s_add_u32 s10, s10, s8
	s_lshl_b32 s8, s39, 7
	s_add_u32 s10, s10, s8
	s_add_u32 s4, s4, s10
	s_addc_u32 s5, s5, 0
	s_lshl_b32 s14, s14, 19
	s_lshr_b32 s8, s39, 2
	s_lshl_b32 s8, s8, 18
	s_add_u32 s14, s14, s8
	s_and_b32 s8, s39, 3
	s_lshl_b32 s8, s8, 15
	s_add_u32 s14, s14, s8
	s_lshl_b32 s8, s11, 17
	s_add_u32 s14, s14, s8
	s_lshl_b32 s8, s38, 7
	s_add_u32 s14, s14, s8
	s_add_u32 s92, s84, s14
	s_addc_u32 s93, s85, 0
	s_movk_i32 s25, 0x400
	s_movk_i32 s27, 0x1000
	s_movk_i32 s8, 0x400
	s_movk_i32 s9, 0x4000
	s_branch .Lcv1_goA1

; #define LAS __attribute__((address_space(3)))
; __device__ __forceinline__ void convert_experts(Frame& F, int lo, int hi) {
;     const int gw = F.vcu * 8 + F.wave, NGW = F.G * 8;
;     LAS unsigned char* scr = F.lds + F.wave * 16384;
;     unsigned char* W1t = WSP(F, WS_W1T, unsigned char); unsigned char* W2t = WSP(F, WS_W2T, unsigned char);
;     const float* weg = F.a->in[I_WEG]; const float* weu = F.a->in[I_WEU]; const float* wed = F.a->in[I_WED];
;     const float* wsg = F.a->in[I_WSG]; const float* wsu = F.a->in[I_WSU]; const float* wsd = F.a->in[I_WSD];
;     ...
;     constexpr int NPAIRS = CONV_ITEMS / 2;
;     (void)lo; (void)hi;
.Lcva_vcu:
	s_lshr_b32 s99, s99, 6
	s_lshl_b32 s101, s101, 3
	s_add_u32 s89, s101, s99
	s_movk_i32 s90, 24
	s_lshr_b32 s32, s89, 3
	s_and_b32 s32, s32, 3
	s_cmp_ge_u32 s32, 2
	s_cselect_b32 s99, 2, 0
	s_sub_u32 s32, s32, s99
	s_mov_b32 s95, 0
	s_waitcnt vmcnt(0)
	s_branch .LBB0_304

; #define LAS __attribute__((address_space(3)))
; __device__ __forceinline__ void lds_barrier() { asm volatile("s_waitcnt lgkmcnt(0)\n\ts_barrier" ::: "memory"); }
; __device__ __forceinline__ void convert_experts(Frame& F, int lo, int hi) {
;     ...
;     constexpr int NPAIRS = CONV_ITEMS / 2;
;     (void)lo; (void)hi;
; __device__ __forceinline__ void phase_attn(Frame& F) {
;     ...
;         lds_barrier();
;         LAS unsigned char* kb = F.lds + buf * ABUF;
;         const bf16x8 q0 = qn0, q1 = qn1;
;         {
;             LAS unsigned char* ob = F.lds + (buf ^ 1) * ABUF;
; #pragma unroll
;             for (int jj = 0; jj < 4; ++jj) { const int ch = tid + 512 * jj, row = ch >> 3, c16 = ch & 7;
;                 *(LAS u32x4*)(ob + row * ATT_ROWB + c16 * 16) = kr[jj]; *(LAS u32x4*)(ob + ATT_VOFF + row * ATT_ROWB + c16 * 16) = vr[jj]; }
;         }
;         const AttnUnit nu = un;
;         un = attn_decode(x8 * PER_X + (jl + 2 * G8 < jlast ? jl + 2 * G8 : jlast)); attn_issue(qkv, un, tid, kr, vr);
;         { const char* qb = (const char*)qkv + (((size_t)nu.b * SEQ + nu.r) * NPROJ + nu.h * 64) * 2; const unsigned qo = __umul24((unsigned)(128 * nu.n + ql), (unsigned)nu.d * (NPROJ * 2)) + 16u * fq;
;           qn0 = *(const bf16x8*)(qb + qo); qn1 = *(const bf16x8*)(qb + qo + 64); }
;         const unsigned qrow = __umul24((unsigned)(128 * cu.n + ql), (unsigned)cu.d);
;         const float c1 = 0.125f * LOG2E;
;         const float nc2 = -__builtin_amdgcn_exp2f(-(float)(cu.h + 1)) * (float)cu.d * LOG2E;
;         const bool first = cu.n == 0;
;         f32x4 St[9];
;         const f32x4 eb = (f32x4){ef[0], ef[1], ef[2], ef[3]} * nc2;
;         float mx = -INFINITY;
;         bf16x8 kf[9][2];
; #pragma unroll
;         for (int T = 0; T < 9; ++T) { LAS unsigned char* ka = kb + (16 * (w + T) + fr) * ATT_ROWB + fq * 16; kf[T][0] = *(LAS bf16x8*)ka; kf[T][1] = *(LAS bf16x8*)(ka + 64); }
.Lcva_wd:
	v_mov_b64_e32 v[48:49], v[4:5]
	v_mov_b64_e32 v[46:47], v[2:3]
	v_mov_b64_e32 v[44:45], v[8:9]
	v_mov_b64_e32 v[42:43], v[6:7]
	s_lshl_b32 s65, 1, s35
	s_waitcnt lgkmcnt(0)
	s_barrier
	s_add_i32 s37, s30, 1
	v_cvt_f32_u32_e32 v54, s37
	v_cvt_f32_u32_e32 v55, s65
	v_add_u32_e32 v110, s85, v82
	v_add_u32_e32 v58, v110, v90
	v_exp_f32_e64 v54, -v54
	v_add_u32_e32 v66, v110, v91
	v_add_u32_e32 v74, v110, v92
	v_add_u32_e32 v111, v110, v93
	v_mul_f32_e32 v79, v55, v54
	ds_read_b128 v[54:57], v58
	ds_read_b128 v[58:61], v58 offset:64
	ds_read_b128 v[62:65], v66
	ds_read_b128 v[66:69], v66 offset:64
	ds_read_b128 v[70:73], v74
	ds_read_b128 v[74:77], v74 offset:64
	ds_read_b128 v[112:115], v111
	ds_read_b128 v[116:119], v111 offset:64
	v_add_u32_e32 v111, v110, v94
	ds_read_b128 v[120:123], v111
	ds_read_b128 v[124:127], v111 offset:64
	v_add_u32_e32 v111, v110, v95
	ds_read_b128 v[128:131], v111
	ds_read_b128 v[132:135], v111 offset:64
	v_add_u32_e32 v111, v110, v96
	ds_read_b128 v[136:139], v111
	ds_read_b128 v[140:143], v111 offset:64
	v_add_u32_e32 v111, v110, v97
	v_add_u32_e32 v110, v110, v98
	ds_read_b128 v[144:147], v111
	ds_read_b128 v[148:151], v111 offset:64
	ds_read_b128 v[152:155], v110
	ds_read_b128 v[156:159], v110 offset:64
	s_sub_u32 s32, s32, 1
	s_cmp_lt_i32 s32, 0
	s_cbranch_scc0 .Lcva_none_l
	s_mov_b32 s32, 1
	s_cmp_eq_u32 s90, 0
	s_cbranch_scc1 .Lcva_none_l
	s_sub_u32 s90, s90, 1
	s_lshr_b32 s98, s89, 6
	s_and_b32 s99, s89, 63
	s_mul_hi_u32 s100, s98, 0xaaaaaaab
	s_lshr_b32 s100, s100, 1
	s_mul_i32 s101, s100, 3
	s_sub_u32 s101, s98, s101
	s_cmp_lt_u32 s100, 256
	s_cselect_b32 s98, 0, 3
	s_cselect_b32 s95, s100, 0
	s_add_u32 s98, s98, s101
	s_lshl_b32 s98, s98, 1
	v_readlane_b32 s96, v253, s98
	s_add_u32 s98, s98, 1
	v_readlane_b32 s97, v253, s98
	s_lshl_b32 s95, s95, 20
	s_nop 3
	s_add_u32 s96, s96, s95
	s_addc_u32 s97, s97, 0
	s_cmp_eq_u32 s101, 2
	s_cbranch_scc1 .Lcva_down_l
	s_lshr_b32 s95, s99, 3
	s_and_b32 s99, s99, 7
	s_lshl_b32 s98, s95, 17
	s_add_u32 s96, s96, s98
	s_addc_u32 s97, s97, 0
	s_lshl_b32 s98, s99, 7
	s_add_u32 s96, s96, s98
	s_addc_u32 s97, s97, 0
	s_lshl_b32 s100, s100, 19
	s_lshr_b32 s98, s99, 2
	s_lshl_b32 s98, s98, 18
	s_add_u32 s100, s100, s98
	s_and_b32 s98, s99, 3
	s_lshl_b32 s98, s98, 15
	s_add_u32 s100, s100, s98
	s_lshl_b32 s98, s101, 17
	s_add_u32 s100, s100, s98
	s_lshl_b32 s98, s95, 7
	s_add_u32 s100, s100, s98
	v_readlane_b32 s92, v253, 12
	v_readlane_b32 s93, v253, 13
	s_mov_b32 s94, 0xc3317218
	s_cmp_eq_u32 s101, 0
	s_cselect_b32 s94, 0xc2b8aa3b, s94
	s_nop 3
	s_add_u32 s92, s92, s100
	s_addc_u32 s93, s93, 0
	s_movk_i32 s95, 0x400
	s_movk_i32 s98, 0x400
	s_branch .Lcva_go_l
